# speedup vs baseline: 1.0312x; 1.0312x over previous
.LBB2_6:
	s_load_dwordx2 s[20:21], s[0:1], 0x0
	s_load_dwordx4 s[24:27], s[0:1], 0x10
	s_mov_b32 s16, s10
	s_mov_b32 s17, s9
	v_mov_b32_e32 v69, v130
	s_lshl_b32 s18, s16, 18
	s_lshl_b32 s19, s17, 17
	s_add_u32 s18, s18, s19
	v_lshl_or_b32 v68, s17, 13, v69
	v_lshlrev_b32_e32 v2, 2, v0
	s_lshl_b32 s28, s16, 9
	s_waitcnt lgkmcnt(0)
	s_add_u32 s20, s20, s18
	s_addc_u32 s21, s21, 0
	s_add_u32 s22, s20, 0x10000
	s_addc_u32 s23, s21, 0
	s_add_u32 s24, s24, s28
	s_addc_u32 s25, s25, 0
	s_add_u32 s26, s26, s28
	s_addc_u32 s27, s27, 0
	global_load_dword v1, v2, s[24:25] offset:-1024
	global_load_dword v3, v2, s[26:27] offset:-1024
	global_load_dwordx4 v[4:7], v69, s[20:21]
	global_load_dwordx4 v[8:11], v69, s[20:21] offset:1024
	global_load_dwordx4 v[12:15], v69, s[20:21] offset:2048
	global_load_dwordx4 v[16:19], v69, s[20:21] offset:3072
	global_load_dwordx4 v[20:23], v69, s[22:23]
	global_load_dwordx4 v[24:27], v69, s[22:23] offset:1024
	global_load_dwordx4 v[28:31], v69, s[22:23] offset:2048
	global_load_dwordx4 v[32:35], v69, s[22:23] offset:3072
	s_add_u32 s20, s20, 0x1000
	s_addc_u32 s21, s21, 0
	s_add_u32 s22, s22, 0x1000
	s_addc_u32 s23, s23, 0
	global_load_dwordx4 v[36:39], v69, s[20:21]
	global_load_dwordx4 v[40:43], v69, s[20:21] offset:1024
	global_load_dwordx4 v[44:47], v69, s[20:21] offset:2048
	global_load_dwordx4 v[48:51], v69, s[20:21] offset:3072
	global_load_dwordx4 v[52:55], v69, s[22:23]
	global_load_dwordx4 v[56:59], v69, s[22:23] offset:1024
	global_load_dwordx4 v[60:63], v69, s[22:23] offset:2048
	global_load_dwordx4 v[64:67], v69, s[22:23] offset:3072
	s_add_u32 s20, s20, 0x1000
	s_addc_u32 s21, s21, 0
	s_add_u32 s22, s22, 0x1000
	s_addc_u32 s23, s23, 0
	s_waitcnt vmcnt(16)
	v_mul_f32_e32 v1, 0x4038aa3b, v1
	ds_write2st64_b32 v2, v1, v3 offset0:124 offset1:126
	s_waitcnt vmcnt(15)
	ds_write_b128 v68, v[4:7]
	s_waitcnt vmcnt(14)
	ds_write_b128 v68, v[8:11] offset:1024
	s_waitcnt vmcnt(13)
	ds_write_b128 v68, v[12:15] offset:2048
	s_waitcnt vmcnt(12)
	ds_write_b128 v68, v[16:19] offset:3072
	s_waitcnt vmcnt(11)
	ds_write_b128 v68, v[20:23] offset:4096
	s_waitcnt vmcnt(10)
	ds_write_b128 v68, v[24:27] offset:5120
	s_waitcnt vmcnt(9)
	ds_write_b128 v68, v[28:31] offset:6144
	s_waitcnt vmcnt(8)
	ds_write_b128 v68, v[32:35] offset:7168
	s_waitcnt lgkmcnt(0)
	s_barrier
	global_load_dwordx4 v[4:7], v69, s[20:21]
	global_load_dwordx4 v[8:11], v69, s[20:21] offset:1024
	global_load_dwordx4 v[12:15], v69, s[20:21] offset:2048
	global_load_dwordx4 v[16:19], v69, s[20:21] offset:3072
	global_load_dwordx4 v[20:23], v69, s[22:23]
	global_load_dwordx4 v[24:27], v69, s[22:23] offset:1024
	global_load_dwordx4 v[28:31], v69, s[22:23] offset:2048
	global_load_dwordx4 v[32:35], v69, s[22:23] offset:3072
	s_add_u32 s20, s20, 0x1000
	s_addc_u32 s21, s21, 0
	s_add_u32 s22, s22, 0x1000
	s_addc_u32 s23, s23, 0
	s_waitcnt vmcnt(15)
	ds_write_b128 v68, v[36:39] offset:16384
	s_waitcnt vmcnt(14)
	ds_write_b128 v68, v[40:43] offset:17408
	s_waitcnt vmcnt(13)
	ds_write_b128 v68, v[44:47] offset:18432
	s_waitcnt vmcnt(12)
	ds_write_b128 v68, v[48:51] offset:19456
	s_waitcnt vmcnt(11)
	ds_write_b128 v68, v[52:55] offset:20480
	s_waitcnt vmcnt(10)
	ds_write_b128 v68, v[56:59] offset:21504
	s_waitcnt vmcnt(9)
	ds_write_b128 v68, v[60:63] offset:22528
	s_waitcnt vmcnt(8)
	ds_write_b128 v68, v[64:67] offset:23552
	s_waitcnt lgkmcnt(0)
	s_barrier
	global_load_dwordx4 v[36:39], v69, s[20:21]
	global_load_dwordx4 v[40:43], v69, s[20:21] offset:1024
	global_load_dwordx4 v[44:47], v69, s[20:21] offset:2048
	global_load_dwordx4 v[48:51], v69, s[20:21] offset:3072
	global_load_dwordx4 v[52:55], v69, s[22:23]
	global_load_dwordx4 v[56:59], v69, s[22:23] offset:1024
	global_load_dwordx4 v[60:63], v69, s[22:23] offset:2048
	global_load_dwordx4 v[64:67], v69, s[22:23] offset:3072
	s_add_u32 s20, s20, 0x1000
	s_addc_u32 s21, s21, 0
	s_add_u32 s22, s22, 0x1000
	s_addc_u32 s23, s23, 0
	s_waitcnt vmcnt(15)
	ds_write_b128 v68, v[4:7]
	s_waitcnt vmcnt(14)
	ds_write_b128 v68, v[8:11] offset:1024
	s_waitcnt vmcnt(13)
	ds_write_b128 v68, v[12:15] offset:2048
	s_waitcnt vmcnt(12)
	ds_write_b128 v68, v[16:19] offset:3072
	s_waitcnt vmcnt(11)
	ds_write_b128 v68, v[20:23] offset:4096
	s_waitcnt vmcnt(10)
	ds_write_b128 v68, v[24:27] offset:5120
	s_waitcnt vmcnt(9)
	ds_write_b128 v68, v[28:31] offset:6144
	s_waitcnt vmcnt(8)
	ds_write_b128 v68, v[32:35] offset:7168
	s_waitcnt lgkmcnt(0)
	s_barrier
	global_load_dwordx4 v[4:7], v69, s[20:21]
	global_load_dwordx4 v[8:11], v69, s[20:21] offset:1024
	global_load_dwordx4 v[12:15], v69, s[20:21] offset:2048
	global_load_dwordx4 v[16:19], v69, s[20:21] offset:3072
	global_load_dwordx4 v[20:23], v69, s[22:23]
	global_load_dwordx4 v[24:27], v69, s[22:23] offset:1024
	global_load_dwordx4 v[28:31], v69, s[22:23] offset:2048
	global_load_dwordx4 v[32:35], v69, s[22:23] offset:3072
	s_add_u32 s20, s20, 0x1000
	s_addc_u32 s21, s21, 0
	s_add_u32 s22, s22, 0x1000
	s_addc_u32 s23, s23, 0
	s_waitcnt vmcnt(15)
	ds_write_b128 v68, v[36:39] offset:16384
	s_waitcnt vmcnt(14)
	ds_write_b128 v68, v[40:43] offset:17408
	s_waitcnt vmcnt(13)
	ds_write_b128 v68, v[44:47] offset:18432
	s_waitcnt vmcnt(12)
	ds_write_b128 v68, v[48:51] offset:19456
	s_waitcnt vmcnt(11)
	ds_write_b128 v68, v[52:55] offset:20480
	s_waitcnt vmcnt(10)
	ds_write_b128 v68, v[56:59] offset:21504
	s_waitcnt vmcnt(9)
	ds_write_b128 v68, v[60:63] offset:22528
	s_waitcnt vmcnt(8)
	ds_write_b128 v68, v[64:67] offset:23552
	s_waitcnt lgkmcnt(0)
	s_barrier
	global_load_dwordx4 v[36:39], v69, s[20:21]
	global_load_dwordx4 v[40:43], v69, s[20:21] offset:1024
	global_load_dwordx4 v[44:47], v69, s[20:21] offset:2048
	global_load_dwordx4 v[48:51], v69, s[20:21] offset:3072
	global_load_dwordx4 v[52:55], v69, s[22:23]
	global_load_dwordx4 v[56:59], v69, s[22:23] offset:1024
	global_load_dwordx4 v[60:63], v69, s[22:23] offset:2048
	global_load_dwordx4 v[64:67], v69, s[22:23] offset:3072
	s_add_u32 s20, s20, 0x1000
	s_addc_u32 s21, s21, 0
	s_add_u32 s22, s22, 0x1000
	s_addc_u32 s23, s23, 0
	s_waitcnt vmcnt(15)
	ds_write_b128 v68, v[4:7]
	s_waitcnt vmcnt(14)
	ds_write_b128 v68, v[8:11] offset:1024
	s_waitcnt vmcnt(13)
	ds_write_b128 v68, v[12:15] offset:2048
	s_waitcnt vmcnt(12)
	ds_write_b128 v68, v[16:19] offset:3072
	s_waitcnt vmcnt(11)
	ds_write_b128 v68, v[20:23] offset:4096
	s_waitcnt vmcnt(10)
	ds_write_b128 v68, v[24:27] offset:5120
	s_waitcnt vmcnt(9)
	ds_write_b128 v68, v[28:31] offset:6144
	s_waitcnt vmcnt(8)
	ds_write_b128 v68, v[32:35] offset:7168
	s_waitcnt lgkmcnt(0)
	s_barrier
	global_load_dwordx4 v[4:7], v69, s[20:21]
	global_load_dwordx4 v[8:11], v69, s[20:21] offset:1024
	global_load_dwordx4 v[12:15], v69, s[20:21] offset:2048
	global_load_dwordx4 v[16:19], v69, s[20:21] offset:3072
	global_load_dwordx4 v[20:23], v69, s[22:23]
	global_load_dwordx4 v[24:27], v69, s[22:23] offset:1024
	global_load_dwordx4 v[28:31], v69, s[22:23] offset:2048
	global_load_dwordx4 v[32:35], v69, s[22:23] offset:3072
	s_add_u32 s20, s20, 0x1000
	s_addc_u32 s21, s21, 0
	s_add_u32 s22, s22, 0x1000
	s_addc_u32 s23, s23, 0
	s_waitcnt vmcnt(15)
	ds_write_b128 v68, v[36:39] offset:16384
	s_waitcnt vmcnt(14)
	ds_write_b128 v68, v[40:43] offset:17408
	s_waitcnt vmcnt(13)
	ds_write_b128 v68, v[44:47] offset:18432
	s_waitcnt vmcnt(12)
	ds_write_b128 v68, v[48:51] offset:19456
	s_waitcnt vmcnt(11)
	ds_write_b128 v68, v[52:55] offset:20480
	s_waitcnt vmcnt(10)
	ds_write_b128 v68, v[56:59] offset:21504
	s_waitcnt vmcnt(9)
	ds_write_b128 v68, v[60:63] offset:22528
	s_waitcnt vmcnt(8)
	ds_write_b128 v68, v[64:67] offset:23552
	s_waitcnt lgkmcnt(0)
	s_barrier
	global_load_dwordx4 v[36:39], v69, s[20:21]
	global_load_dwordx4 v[40:43], v69, s[20:21] offset:1024
	global_load_dwordx4 v[44:47], v69, s[20:21] offset:2048
	global_load_dwordx4 v[48:51], v69, s[20:21] offset:3072
	global_load_dwordx4 v[52:55], v69, s[22:23]
	global_load_dwordx4 v[56:59], v69, s[22:23] offset:1024
	global_load_dwordx4 v[60:63], v69, s[22:23] offset:2048
	global_load_dwordx4 v[64:67], v69, s[22:23] offset:3072
	s_add_u32 s20, s20, 0x1000
	s_addc_u32 s21, s21, 0
	s_add_u32 s22, s22, 0x1000
	s_addc_u32 s23, s23, 0
	s_waitcnt vmcnt(15)
	ds_write_b128 v68, v[4:7]
	s_waitcnt vmcnt(14)
	ds_write_b128 v68, v[8:11] offset:1024
	s_waitcnt vmcnt(13)
	ds_write_b128 v68, v[12:15] offset:2048
	s_waitcnt vmcnt(12)
	ds_write_b128 v68, v[16:19] offset:3072
	s_waitcnt vmcnt(11)
	ds_write_b128 v68, v[20:23] offset:4096
	s_waitcnt vmcnt(10)
	ds_write_b128 v68, v[24:27] offset:5120
	s_waitcnt vmcnt(9)
	ds_write_b128 v68, v[28:31] offset:6144
	s_waitcnt vmcnt(8)
	ds_write_b128 v68, v[32:35] offset:7168
	s_waitcnt lgkmcnt(0)
	s_barrier
	global_load_dwordx4 v[4:7], v69, s[20:21]
	global_load_dwordx4 v[8:11], v69, s[20:21] offset:1024
	global_load_dwordx4 v[12:15], v69, s[20:21] offset:2048
	global_load_dwordx4 v[16:19], v69, s[20:21] offset:3072
	global_load_dwordx4 v[20:23], v69, s[22:23]
	global_load_dwordx4 v[24:27], v69, s[22:23] offset:1024
	global_load_dwordx4 v[28:31], v69, s[22:23] offset:2048
	global_load_dwordx4 v[32:35], v69, s[22:23] offset:3072
	s_add_u32 s20, s20, 0x1000
	s_addc_u32 s21, s21, 0
	s_add_u32 s22, s22, 0x1000
	s_addc_u32 s23, s23, 0
	s_waitcnt vmcnt(15)
	ds_write_b128 v68, v[36:39] offset:16384
	s_waitcnt vmcnt(14)
	ds_write_b128 v68, v[40:43] offset:17408
	s_waitcnt vmcnt(13)
	ds_write_b128 v68, v[44:47] offset:18432
	s_waitcnt vmcnt(12)
	ds_write_b128 v68, v[48:51] offset:19456
	s_waitcnt vmcnt(11)
	ds_write_b128 v68, v[52:55] offset:20480
	s_waitcnt vmcnt(10)
	ds_write_b128 v68, v[56:59] offset:21504
	s_waitcnt vmcnt(9)
	ds_write_b128 v68, v[60:63] offset:22528
	s_waitcnt vmcnt(8)
	ds_write_b128 v68, v[64:67] offset:23552
	s_waitcnt lgkmcnt(0)
	s_barrier
	global_load_dwordx4 v[36:39], v69, s[20:21]
	global_load_dwordx4 v[40:43], v69, s[20:21] offset:1024
	global_load_dwordx4 v[44:47], v69, s[20:21] offset:2048
	global_load_dwordx4 v[48:51], v69, s[20:21] offset:3072
	global_load_dwordx4 v[52:55], v69, s[22:23]
	global_load_dwordx4 v[56:59], v69, s[22:23] offset:1024
	global_load_dwordx4 v[60:63], v69, s[22:23] offset:2048
	global_load_dwordx4 v[64:67], v69, s[22:23] offset:3072
	s_add_u32 s20, s20, 0x1000
	s_addc_u32 s21, s21, 0
	s_add_u32 s22, s22, 0x1000
	s_addc_u32 s23, s23, 0
	s_waitcnt vmcnt(15)
	ds_write_b128 v68, v[4:7]
	s_waitcnt vmcnt(14)
	ds_write_b128 v68, v[8:11] offset:1024
	s_waitcnt vmcnt(13)
	ds_write_b128 v68, v[12:15] offset:2048
	s_waitcnt vmcnt(12)
	ds_write_b128 v68, v[16:19] offset:3072
	s_waitcnt vmcnt(11)
	ds_write_b128 v68, v[20:23] offset:4096
	s_waitcnt vmcnt(10)
	ds_write_b128 v68, v[24:27] offset:5120
	s_waitcnt vmcnt(9)
	ds_write_b128 v68, v[28:31] offset:6144
	s_waitcnt vmcnt(8)
	ds_write_b128 v68, v[32:35] offset:7168
	s_waitcnt lgkmcnt(0)
	s_barrier
	global_load_dwordx4 v[4:7], v69, s[20:21]
	global_load_dwordx4 v[8:11], v69, s[20:21] offset:1024
	global_load_dwordx4 v[12:15], v69, s[20:21] offset:2048
	global_load_dwordx4 v[16:19], v69, s[20:21] offset:3072
	global_load_dwordx4 v[20:23], v69, s[22:23]
	global_load_dwordx4 v[24:27], v69, s[22:23] offset:1024
	global_load_dwordx4 v[28:31], v69, s[22:23] offset:2048
	global_load_dwordx4 v[32:35], v69, s[22:23] offset:3072
	s_add_u32 s20, s20, 0x1000
	s_addc_u32 s21, s21, 0
	s_add_u32 s22, s22, 0x1000
	s_addc_u32 s23, s23, 0
	s_waitcnt vmcnt(15)
	ds_write_b128 v68, v[36:39] offset:16384
	s_waitcnt vmcnt(14)
	ds_write_b128 v68, v[40:43] offset:17408
	s_waitcnt vmcnt(13)
	ds_write_b128 v68, v[44:47] offset:18432
	s_waitcnt vmcnt(12)
	ds_write_b128 v68, v[48:51] offset:19456
	s_waitcnt vmcnt(11)
	ds_write_b128 v68, v[52:55] offset:20480
	s_waitcnt vmcnt(10)
	ds_write_b128 v68, v[56:59] offset:21504
	s_waitcnt vmcnt(9)
	ds_write_b128 v68, v[60:63] offset:22528
	s_waitcnt vmcnt(8)
	ds_write_b128 v68, v[64:67] offset:23552
	s_waitcnt lgkmcnt(0)
	s_barrier
	global_load_dwordx4 v[36:39], v69, s[20:21]
	global_load_dwordx4 v[40:43], v69, s[20:21] offset:1024
	global_load_dwordx4 v[44:47], v69, s[20:21] offset:2048
	global_load_dwordx4 v[48:51], v69, s[20:21] offset:3072
	global_load_dwordx4 v[52:55], v69, s[22:23]
	global_load_dwordx4 v[56:59], v69, s[22:23] offset:1024
	global_load_dwordx4 v[60:63], v69, s[22:23] offset:2048
	global_load_dwordx4 v[64:67], v69, s[22:23] offset:3072
	s_add_u32 s20, s20, 0x1000
	s_addc_u32 s21, s21, 0
	s_add_u32 s22, s22, 0x1000
	s_addc_u32 s23, s23, 0
	s_waitcnt vmcnt(15)
	ds_write_b128 v68, v[4:7]
	s_waitcnt vmcnt(14)
	ds_write_b128 v68, v[8:11] offset:1024
	s_waitcnt vmcnt(13)
	ds_write_b128 v68, v[12:15] offset:2048
	s_waitcnt vmcnt(12)
	ds_write_b128 v68, v[16:19] offset:3072
	s_waitcnt vmcnt(11)
	ds_write_b128 v68, v[20:23] offset:4096
	s_waitcnt vmcnt(10)
	ds_write_b128 v68, v[24:27] offset:5120
	s_waitcnt vmcnt(9)
	ds_write_b128 v68, v[28:31] offset:6144
	s_waitcnt vmcnt(8)
	ds_write_b128 v68, v[32:35] offset:7168
	s_waitcnt lgkmcnt(0)
	s_barrier
	global_load_dwordx4 v[4:7], v69, s[20:21]
	global_load_dwordx4 v[8:11], v69, s[20:21] offset:1024
	global_load_dwordx4 v[12:15], v69, s[20:21] offset:2048
	global_load_dwordx4 v[16:19], v69, s[20:21] offset:3072
	global_load_dwordx4 v[20:23], v69, s[22:23]
	global_load_dwordx4 v[24:27], v69, s[22:23] offset:1024
	global_load_dwordx4 v[28:31], v69, s[22:23] offset:2048
	global_load_dwordx4 v[32:35], v69, s[22:23] offset:3072
	s_add_u32 s20, s20, 0x1000
	s_addc_u32 s21, s21, 0
	s_add_u32 s22, s22, 0x1000
	s_addc_u32 s23, s23, 0
	s_waitcnt vmcnt(15)
	ds_write_b128 v68, v[36:39] offset:16384
	s_waitcnt vmcnt(14)
	ds_write_b128 v68, v[40:43] offset:17408
	s_waitcnt vmcnt(13)
	ds_write_b128 v68, v[44:47] offset:18432
	s_waitcnt vmcnt(12)
	ds_write_b128 v68, v[48:51] offset:19456
	s_waitcnt vmcnt(11)
	ds_write_b128 v68, v[52:55] offset:20480
	s_waitcnt vmcnt(10)
	ds_write_b128 v68, v[56:59] offset:21504
	s_waitcnt vmcnt(9)
	ds_write_b128 v68, v[60:63] offset:22528
	s_waitcnt vmcnt(8)
	ds_write_b128 v68, v[64:67] offset:23552
	s_waitcnt lgkmcnt(0)
	s_barrier
	global_load_dwordx4 v[36:39], v69, s[20:21]
	global_load_dwordx4 v[40:43], v69, s[20:21] offset:1024
	global_load_dwordx4 v[44:47], v69, s[20:21] offset:2048
	global_load_dwordx4 v[48:51], v69, s[20:21] offset:3072
	global_load_dwordx4 v[52:55], v69, s[22:23]
	global_load_dwordx4 v[56:59], v69, s[22:23] offset:1024
	global_load_dwordx4 v[60:63], v69, s[22:23] offset:2048
	global_load_dwordx4 v[64:67], v69, s[22:23] offset:3072
	s_add_u32 s20, s20, 0x1000
	s_addc_u32 s21, s21, 0
	s_add_u32 s22, s22, 0x1000
	s_addc_u32 s23, s23, 0
	s_waitcnt vmcnt(15)
	ds_write_b128 v68, v[4:7]
	s_waitcnt vmcnt(14)
	ds_write_b128 v68, v[8:11] offset:1024
	s_waitcnt vmcnt(13)
	ds_write_b128 v68, v[12:15] offset:2048
	s_waitcnt vmcnt(12)
	ds_write_b128 v68, v[16:19] offset:3072
	s_waitcnt vmcnt(11)
	ds_write_b128 v68, v[20:23] offset:4096
	s_waitcnt vmcnt(10)
	ds_write_b128 v68, v[24:27] offset:5120
	s_waitcnt vmcnt(9)
	ds_write_b128 v68, v[28:31] offset:6144
	s_waitcnt vmcnt(8)
	ds_write_b128 v68, v[32:35] offset:7168
	s_waitcnt lgkmcnt(0)
	s_barrier
	global_load_dwordx4 v[4:7], v69, s[20:21]
	global_load_dwordx4 v[8:11], v69, s[20:21] offset:1024
	global_load_dwordx4 v[12:15], v69, s[20:21] offset:2048
	global_load_dwordx4 v[16:19], v69, s[20:21] offset:3072
	global_load_dwordx4 v[20:23], v69, s[22:23]
	global_load_dwordx4 v[24:27], v69, s[22:23] offset:1024
	global_load_dwordx4 v[28:31], v69, s[22:23] offset:2048
	global_load_dwordx4 v[32:35], v69, s[22:23] offset:3072
	s_add_u32 s20, s20, 0x1000
	s_addc_u32 s21, s21, 0
	s_add_u32 s22, s22, 0x1000
	s_addc_u32 s23, s23, 0
	s_waitcnt vmcnt(15)
	ds_write_b128 v68, v[36:39] offset:16384
	s_waitcnt vmcnt(14)
	ds_write_b128 v68, v[40:43] offset:17408
	s_waitcnt vmcnt(13)
	ds_write_b128 v68, v[44:47] offset:18432
	s_waitcnt vmcnt(12)
	ds_write_b128 v68, v[48:51] offset:19456
	s_waitcnt vmcnt(11)
	ds_write_b128 v68, v[52:55] offset:20480
	s_waitcnt vmcnt(10)
	ds_write_b128 v68, v[56:59] offset:21504
	s_waitcnt vmcnt(9)
	ds_write_b128 v68, v[60:63] offset:22528
	s_waitcnt vmcnt(8)
	ds_write_b128 v68, v[64:67] offset:23552
	s_waitcnt lgkmcnt(0)
	s_barrier
	global_load_dwordx4 v[36:39], v69, s[20:21]
	global_load_dwordx4 v[40:43], v69, s[20:21] offset:1024
	global_load_dwordx4 v[44:47], v69, s[20:21] offset:2048
	global_load_dwordx4 v[48:51], v69, s[20:21] offset:3072
	global_load_dwordx4 v[52:55], v69, s[22:23]
	global_load_dwordx4 v[56:59], v69, s[22:23] offset:1024
	global_load_dwordx4 v[60:63], v69, s[22:23] offset:2048
	global_load_dwordx4 v[64:67], v69, s[22:23] offset:3072
	s_add_u32 s20, s20, 0x1000
	s_addc_u32 s21, s21, 0
	s_add_u32 s22, s22, 0x1000
	s_addc_u32 s23, s23, 0
	s_waitcnt vmcnt(15)
	ds_write_b128 v68, v[4:7]
	s_waitcnt vmcnt(14)
	ds_write_b128 v68, v[8:11] offset:1024
	s_waitcnt vmcnt(13)
	ds_write_b128 v68, v[12:15] offset:2048
	s_waitcnt vmcnt(12)
	ds_write_b128 v68, v[16:19] offset:3072
	s_waitcnt vmcnt(11)
	ds_write_b128 v68, v[20:23] offset:4096
	s_waitcnt vmcnt(10)
	ds_write_b128 v68, v[24:27] offset:5120
	s_waitcnt vmcnt(9)
	ds_write_b128 v68, v[28:31] offset:6144
	s_waitcnt vmcnt(8)
	ds_write_b128 v68, v[32:35] offset:7168
	s_waitcnt lgkmcnt(0)
	s_barrier
	s_waitcnt vmcnt(7)
	ds_write_b128 v68, v[36:39] offset:16384
	s_waitcnt vmcnt(6)
	ds_write_b128 v68, v[40:43] offset:17408
	s_waitcnt vmcnt(5)
	ds_write_b128 v68, v[44:47] offset:18432
	s_waitcnt vmcnt(4)
	ds_write_b128 v68, v[48:51] offset:19456
	s_waitcnt vmcnt(3)
	ds_write_b128 v68, v[52:55] offset:20480
	s_waitcnt vmcnt(2)
	ds_write_b128 v68, v[56:59] offset:21504
	s_waitcnt vmcnt(1)
	ds_write_b128 v68, v[60:63] offset:22528
	s_waitcnt vmcnt(0)
	ds_write_b128 v68, v[64:67] offset:23552
	s_waitcnt lgkmcnt(0)
	s_barrier
	s_endpgm
	s_nop 0
	s_nop 0
	s_nop 0
	s_nop 0
	s_nop 0
	s_nop 0
	s_nop 0
	s_nop 0
	s_nop 0
	s_nop 0
	s_nop 0
	s_nop 0
	s_nop 0
	s_nop 0
	s_nop 0
	s_nop 0
	s_nop 0
	s_nop 0
	s_nop 0
	s_nop 0
	s_nop 0
	s_nop 0
	s_nop 0
	s_nop 0
	s_nop 0
	s_nop 0
	s_nop 0
	s_nop 0
	s_nop 0
	s_nop 0
	s_nop 0
	s_nop 0
	s_nop 0
	s_nop 0
	s_nop 0
	s_nop 0
	s_nop 0
	s_nop 0
	s_nop 0
	s_nop 0
	s_nop 0
	s_nop 0
	s_nop 0
	s_nop 0
	s_nop 0
	s_nop 0
	s_nop 0
	s_nop 0
	s_nop 0
	s_nop 0
	s_nop 0
	s_nop 0
	s_nop 0
	s_nop 0
	s_nop 0
	s_nop 0
	s_nop 0
	s_nop 0
	s_endpgm

.LBB3_4:
	s_load_dwordx2 s[20:21], s[0:1], 0x0
	s_load_dwordx2 s[24:25], s[0:1], 0x38
	s_mov_b32 s16, s4
	s_mov_b32 s17, s5
	v_mov_b32_e32 v69, v134
	s_lshl_b32 s18, s16, 18
	s_lshl_b32 s19, s17, 17
	s_add_u32 s18, s18, s19
	v_lshl_or_b32 v68, s17, 13, v69
	v_lshlrev_b32_e32 v2, 4, v0
	s_lshl_b32 s28, s16, 14
	s_waitcnt lgkmcnt(0)
	s_add_u32 s20, s20, s18
	s_addc_u32 s21, s21, 0
	s_add_u32 s22, s20, 0x10000
	s_addc_u32 s23, s21, 0
	s_add_u32 s24, s24, s28
	s_addc_u32 s25, s25, 0
	global_load_dwordx4 v[4:7], v69, s[20:21]
	global_load_dwordx4 v[8:11], v69, s[20:21] offset:1024
	global_load_dwordx4 v[12:15], v69, s[20:21] offset:2048
	global_load_dwordx4 v[16:19], v69, s[20:21] offset:3072
	global_load_dwordx4 v[20:23], v69, s[22:23]
	global_load_dwordx4 v[24:27], v69, s[22:23] offset:1024
	global_load_dwordx4 v[28:31], v69, s[22:23] offset:2048
	global_load_dwordx4 v[32:35], v69, s[22:23] offset:3072
	s_add_u32 s20, s20, 0x1000
	s_addc_u32 s21, s21, 0
	s_add_u32 s22, s22, 0x1000
	s_addc_u32 s23, s23, 0
	global_load_dwordx4 v[36:39], v69, s[20:21]
	global_load_dwordx4 v[40:43], v69, s[20:21] offset:1024
	global_load_dwordx4 v[44:47], v69, s[20:21] offset:2048
	global_load_dwordx4 v[48:51], v69, s[20:21] offset:3072
	global_load_dwordx4 v[52:55], v69, s[22:23]
	global_load_dwordx4 v[56:59], v69, s[22:23] offset:1024
	global_load_dwordx4 v[60:63], v69, s[22:23] offset:2048
	global_load_dwordx4 v[64:67], v69, s[22:23] offset:3072
	s_add_u32 s20, s20, 0x1000
	s_addc_u32 s21, s21, 0
	s_add_u32 s22, s22, 0x1000
	s_addc_u32 s23, s23, 0
	s_waitcnt vmcnt(15)
	ds_write_b128 v68, v[4:7]
	s_waitcnt vmcnt(14)
	ds_write_b128 v68, v[8:11] offset:1024
	s_waitcnt vmcnt(13)
	ds_write_b128 v68, v[12:15] offset:2048
	s_waitcnt vmcnt(12)
	ds_write_b128 v68, v[16:19] offset:3072
	s_waitcnt vmcnt(11)
	ds_write_b128 v68, v[20:23] offset:4096
	s_waitcnt vmcnt(10)
	ds_write_b128 v68, v[24:27] offset:5120
	s_waitcnt vmcnt(9)
	ds_write_b128 v68, v[28:31] offset:6144
	s_waitcnt vmcnt(8)
	ds_write_b128 v68, v[32:35] offset:7168
	s_waitcnt lgkmcnt(0)
	s_barrier
	global_load_dwordx4 v[4:7], v69, s[20:21]
	global_load_dwordx4 v[8:11], v69, s[20:21] offset:1024
	global_load_dwordx4 v[12:15], v69, s[20:21] offset:2048
	global_load_dwordx4 v[16:19], v69, s[20:21] offset:3072
	global_load_dwordx4 v[20:23], v69, s[22:23]
	global_load_dwordx4 v[24:27], v69, s[22:23] offset:1024
	global_load_dwordx4 v[28:31], v69, s[22:23] offset:2048
	global_load_dwordx4 v[32:35], v69, s[22:23] offset:3072
	s_add_u32 s20, s20, 0x1000
	s_addc_u32 s21, s21, 0
	s_add_u32 s22, s22, 0x1000
	s_addc_u32 s23, s23, 0
	s_waitcnt vmcnt(15)
	ds_write_b128 v68, v[36:39] offset:16384
	s_waitcnt vmcnt(14)
	ds_write_b128 v68, v[40:43] offset:17408
	s_waitcnt vmcnt(13)
	ds_write_b128 v68, v[44:47] offset:18432
	s_waitcnt vmcnt(12)
	ds_write_b128 v68, v[48:51] offset:19456
	s_waitcnt vmcnt(11)
	ds_write_b128 v68, v[52:55] offset:20480
	s_waitcnt vmcnt(10)
	ds_write_b128 v68, v[56:59] offset:21504
	s_waitcnt vmcnt(9)
	ds_write_b128 v68, v[60:63] offset:22528
	s_waitcnt vmcnt(8)
	ds_write_b128 v68, v[64:67] offset:23552
	s_waitcnt lgkmcnt(0)
	s_barrier
	global_load_dwordx4 v[36:39], v69, s[20:21]
	global_load_dwordx4 v[40:43], v69, s[20:21] offset:1024
	global_load_dwordx4 v[44:47], v69, s[20:21] offset:2048
	global_load_dwordx4 v[48:51], v69, s[20:21] offset:3072
	global_load_dwordx4 v[52:55], v69, s[22:23]
	global_load_dwordx4 v[56:59], v69, s[22:23] offset:1024
	global_load_dwordx4 v[60:63], v69, s[22:23] offset:2048
	global_load_dwordx4 v[64:67], v69, s[22:23] offset:3072
	s_add_u32 s20, s20, 0x1000
	s_addc_u32 s21, s21, 0
	s_add_u32 s22, s22, 0x1000
	s_addc_u32 s23, s23, 0
	s_waitcnt vmcnt(15)
	ds_write_b128 v68, v[4:7]
	s_waitcnt vmcnt(14)
	ds_write_b128 v68, v[8:11] offset:1024
	s_waitcnt vmcnt(13)
	ds_write_b128 v68, v[12:15] offset:2048
	s_waitcnt vmcnt(12)
	ds_write_b128 v68, v[16:19] offset:3072
	s_waitcnt vmcnt(11)
	ds_write_b128 v68, v[20:23] offset:4096
	s_waitcnt vmcnt(10)
	ds_write_b128 v68, v[24:27] offset:5120
	s_waitcnt vmcnt(9)
	ds_write_b128 v68, v[28:31] offset:6144
	s_waitcnt vmcnt(8)
	ds_write_b128 v68, v[32:35] offset:7168
	s_waitcnt lgkmcnt(0)
	s_barrier
	global_load_dwordx4 v[4:7], v69, s[20:21]
	global_load_dwordx4 v[8:11], v69, s[20:21] offset:1024
	global_load_dwordx4 v[12:15], v69, s[20:21] offset:2048
	global_load_dwordx4 v[16:19], v69, s[20:21] offset:3072
	global_load_dwordx4 v[20:23], v69, s[22:23]
	global_load_dwordx4 v[24:27], v69, s[22:23] offset:1024
	global_load_dwordx4 v[28:31], v69, s[22:23] offset:2048
	global_load_dwordx4 v[32:35], v69, s[22:23] offset:3072
	s_add_u32 s20, s20, 0x1000
	s_addc_u32 s21, s21, 0
	s_add_u32 s22, s22, 0x1000
	s_addc_u32 s23, s23, 0
	s_waitcnt vmcnt(15)
	ds_write_b128 v68, v[36:39] offset:16384
	s_waitcnt vmcnt(14)
	ds_write_b128 v68, v[40:43] offset:17408
	s_waitcnt vmcnt(13)
	ds_write_b128 v68, v[44:47] offset:18432
	s_waitcnt vmcnt(12)
	ds_write_b128 v68, v[48:51] offset:19456
	s_waitcnt vmcnt(11)
	ds_write_b128 v68, v[52:55] offset:20480
	s_waitcnt vmcnt(10)
	ds_write_b128 v68, v[56:59] offset:21504
	s_waitcnt vmcnt(9)
	ds_write_b128 v68, v[60:63] offset:22528
	s_waitcnt vmcnt(8)
	ds_write_b128 v68, v[64:67] offset:23552
	s_waitcnt lgkmcnt(0)
	s_barrier
	global_load_dwordx4 v[36:39], v69, s[20:21]
	global_load_dwordx4 v[40:43], v69, s[20:21] offset:1024
	global_load_dwordx4 v[44:47], v69, s[20:21] offset:2048
	global_load_dwordx4 v[48:51], v69, s[20:21] offset:3072
	global_load_dwordx4 v[52:55], v69, s[22:23]
	global_load_dwordx4 v[56:59], v69, s[22:23] offset:1024
	global_load_dwordx4 v[60:63], v69, s[22:23] offset:2048
	global_load_dwordx4 v[64:67], v69, s[22:23] offset:3072
	s_add_u32 s20, s20, 0x1000
	s_addc_u32 s21, s21, 0
	s_add_u32 s22, s22, 0x1000
	s_addc_u32 s23, s23, 0
	s_waitcnt vmcnt(15)
	ds_write_b128 v68, v[4:7]
	s_waitcnt vmcnt(14)
	ds_write_b128 v68, v[8:11] offset:1024
	s_waitcnt vmcnt(13)
	ds_write_b128 v68, v[12:15] offset:2048
	s_waitcnt vmcnt(12)
	ds_write_b128 v68, v[16:19] offset:3072
	s_waitcnt vmcnt(11)
	ds_write_b128 v68, v[20:23] offset:4096
	s_waitcnt vmcnt(10)
	ds_write_b128 v68, v[24:27] offset:5120
	s_waitcnt vmcnt(9)
	ds_write_b128 v68, v[28:31] offset:6144
	s_waitcnt vmcnt(8)
	ds_write_b128 v68, v[32:35] offset:7168
	s_waitcnt lgkmcnt(0)
	s_barrier
	global_load_dwordx4 v[4:7], v69, s[20:21]
	global_load_dwordx4 v[8:11], v69, s[20:21] offset:1024
	global_load_dwordx4 v[12:15], v69, s[20:21] offset:2048
	global_load_dwordx4 v[16:19], v69, s[20:21] offset:3072
	global_load_dwordx4 v[20:23], v69, s[22:23]
	global_load_dwordx4 v[24:27], v69, s[22:23] offset:1024
	global_load_dwordx4 v[28:31], v69, s[22:23] offset:2048
	global_load_dwordx4 v[32:35], v69, s[22:23] offset:3072
	s_add_u32 s20, s20, 0x1000
	s_addc_u32 s21, s21, 0
	s_add_u32 s22, s22, 0x1000
	s_addc_u32 s23, s23, 0
	s_waitcnt vmcnt(15)
	ds_write_b128 v68, v[36:39] offset:16384
	s_waitcnt vmcnt(14)
	ds_write_b128 v68, v[40:43] offset:17408
	s_waitcnt vmcnt(13)
	ds_write_b128 v68, v[44:47] offset:18432
	s_waitcnt vmcnt(12)
	ds_write_b128 v68, v[48:51] offset:19456
	s_waitcnt vmcnt(11)
	ds_write_b128 v68, v[52:55] offset:20480
	s_waitcnt vmcnt(10)
	ds_write_b128 v68, v[56:59] offset:21504
	s_waitcnt vmcnt(9)
	ds_write_b128 v68, v[60:63] offset:22528
	s_waitcnt vmcnt(8)
	ds_write_b128 v68, v[64:67] offset:23552
	s_waitcnt lgkmcnt(0)
	s_barrier
	global_load_dwordx4 v[36:39], v69, s[20:21]
	global_load_dwordx4 v[40:43], v69, s[20:21] offset:1024
	global_load_dwordx4 v[44:47], v69, s[20:21] offset:2048
	global_load_dwordx4 v[48:51], v69, s[20:21] offset:3072
	global_load_dwordx4 v[52:55], v69, s[22:23]
	global_load_dwordx4 v[56:59], v69, s[22:23] offset:1024
	global_load_dwordx4 v[60:63], v69, s[22:23] offset:2048
	global_load_dwordx4 v[64:67], v69, s[22:23] offset:3072
	s_add_u32 s20, s20, 0x1000
	s_addc_u32 s21, s21, 0
	s_add_u32 s22, s22, 0x1000
	s_addc_u32 s23, s23, 0
	s_waitcnt vmcnt(15)
	ds_write_b128 v68, v[4:7]
	s_waitcnt vmcnt(14)
	ds_write_b128 v68, v[8:11] offset:1024
	s_waitcnt vmcnt(13)
	ds_write_b128 v68, v[12:15] offset:2048
	s_waitcnt vmcnt(12)
	ds_write_b128 v68, v[16:19] offset:3072
	s_waitcnt vmcnt(11)
	ds_write_b128 v68, v[20:23] offset:4096
	s_waitcnt vmcnt(10)
	ds_write_b128 v68, v[24:27] offset:5120
	s_waitcnt vmcnt(9)
	ds_write_b128 v68, v[28:31] offset:6144
	s_waitcnt vmcnt(8)
	ds_write_b128 v68, v[32:35] offset:7168
	s_waitcnt lgkmcnt(0)
	s_barrier
	global_load_dwordx4 v[4:7], v69, s[20:21]
	global_load_dwordx4 v[8:11], v69, s[20:21] offset:1024
	global_load_dwordx4 v[12:15], v69, s[20:21] offset:2048
	global_load_dwordx4 v[16:19], v69, s[20:21] offset:3072
	global_load_dwordx4 v[20:23], v69, s[22:23]
	global_load_dwordx4 v[24:27], v69, s[22:23] offset:1024
	global_load_dwordx4 v[28:31], v69, s[22:23] offset:2048
	global_load_dwordx4 v[32:35], v69, s[22:23] offset:3072
	s_add_u32 s20, s20, 0x1000
	s_addc_u32 s21, s21, 0
	s_add_u32 s22, s22, 0x1000
	s_addc_u32 s23, s23, 0
	s_waitcnt vmcnt(15)
	ds_write_b128 v68, v[36:39] offset:16384
	s_waitcnt vmcnt(14)
	ds_write_b128 v68, v[40:43] offset:17408
	s_waitcnt vmcnt(13)
	ds_write_b128 v68, v[44:47] offset:18432
	s_waitcnt vmcnt(12)
	ds_write_b128 v68, v[48:51] offset:19456
	s_waitcnt vmcnt(11)
	ds_write_b128 v68, v[52:55] offset:20480
	s_waitcnt vmcnt(10)
	ds_write_b128 v68, v[56:59] offset:21504
	s_waitcnt vmcnt(9)
	ds_write_b128 v68, v[60:63] offset:22528
	s_waitcnt vmcnt(8)
	ds_write_b128 v68, v[64:67] offset:23552
	s_waitcnt lgkmcnt(0)
	s_barrier
	global_load_dwordx4 v[36:39], v69, s[20:21]
	global_load_dwordx4 v[40:43], v69, s[20:21] offset:1024
	global_load_dwordx4 v[44:47], v69, s[20:21] offset:2048
	global_load_dwordx4 v[48:51], v69, s[20:21] offset:3072
	global_load_dwordx4 v[52:55], v69, s[22:23]
	global_load_dwordx4 v[56:59], v69, s[22:23] offset:1024
	global_load_dwordx4 v[60:63], v69, s[22:23] offset:2048
	global_load_dwordx4 v[64:67], v69, s[22:23] offset:3072
	s_add_u32 s20, s20, 0x1000
	s_addc_u32 s21, s21, 0
	s_add_u32 s22, s22, 0x1000
	s_addc_u32 s23, s23, 0
	s_waitcnt vmcnt(15)
	ds_write_b128 v68, v[4:7]
	s_waitcnt vmcnt(14)
	ds_write_b128 v68, v[8:11] offset:1024
	s_waitcnt vmcnt(13)
	ds_write_b128 v68, v[12:15] offset:2048
	s_waitcnt vmcnt(12)
	ds_write_b128 v68, v[16:19] offset:3072
	s_waitcnt vmcnt(11)
	ds_write_b128 v68, v[20:23] offset:4096
	s_waitcnt vmcnt(10)
	ds_write_b128 v68, v[24:27] offset:5120
	s_waitcnt vmcnt(9)
	ds_write_b128 v68, v[28:31] offset:6144
	s_waitcnt vmcnt(8)
	ds_write_b128 v68, v[32:35] offset:7168
	s_waitcnt lgkmcnt(0)
	s_barrier
	global_load_dwordx4 v[4:7], v69, s[20:21]
	global_load_dwordx4 v[8:11], v69, s[20:21] offset:1024
	global_load_dwordx4 v[12:15], v69, s[20:21] offset:2048
	global_load_dwordx4 v[16:19], v69, s[20:21] offset:3072
	global_load_dwordx4 v[20:23], v69, s[22:23]
	global_load_dwordx4 v[24:27], v69, s[22:23] offset:1024
	global_load_dwordx4 v[28:31], v69, s[22:23] offset:2048
	global_load_dwordx4 v[32:35], v69, s[22:23] offset:3072
	s_add_u32 s20, s20, 0x1000
	s_addc_u32 s21, s21, 0
	s_add_u32 s22, s22, 0x1000
	s_addc_u32 s23, s23, 0
	s_waitcnt vmcnt(15)
	ds_write_b128 v68, v[36:39] offset:16384
	s_waitcnt vmcnt(14)
	ds_write_b128 v68, v[40:43] offset:17408
	s_waitcnt vmcnt(13)
	ds_write_b128 v68, v[44:47] offset:18432
	s_waitcnt vmcnt(12)
	ds_write_b128 v68, v[48:51] offset:19456
	s_waitcnt vmcnt(11)
	ds_write_b128 v68, v[52:55] offset:20480
	s_waitcnt vmcnt(10)
	ds_write_b128 v68, v[56:59] offset:21504
	s_waitcnt vmcnt(9)
	ds_write_b128 v68, v[60:63] offset:22528
	s_waitcnt vmcnt(8)
	ds_write_b128 v68, v[64:67] offset:23552
	s_waitcnt lgkmcnt(0)
	s_barrier
	global_load_dwordx4 v[36:39], v69, s[20:21]
	global_load_dwordx4 v[40:43], v69, s[20:21] offset:1024
	global_load_dwordx4 v[44:47], v69, s[20:21] offset:2048
	global_load_dwordx4 v[48:51], v69, s[20:21] offset:3072
	global_load_dwordx4 v[52:55], v69, s[22:23]
	global_load_dwordx4 v[56:59], v69, s[22:23] offset:1024
	global_load_dwordx4 v[60:63], v69, s[22:23] offset:2048
	global_load_dwordx4 v[64:67], v69, s[22:23] offset:3072
	s_add_u32 s20, s20, 0x1000
	s_addc_u32 s21, s21, 0
	s_add_u32 s22, s22, 0x1000
	s_addc_u32 s23, s23, 0
	s_waitcnt vmcnt(15)
	ds_write_b128 v68, v[4:7]
	s_waitcnt vmcnt(14)
	ds_write_b128 v68, v[8:11] offset:1024
	s_waitcnt vmcnt(13)
	ds_write_b128 v68, v[12:15] offset:2048
	s_waitcnt vmcnt(12)
	ds_write_b128 v68, v[16:19] offset:3072
	s_waitcnt vmcnt(11)
	ds_write_b128 v68, v[20:23] offset:4096
	s_waitcnt vmcnt(10)
	ds_write_b128 v68, v[24:27] offset:5120
	s_waitcnt vmcnt(9)
	ds_write_b128 v68, v[28:31] offset:6144
	s_waitcnt vmcnt(8)
	ds_write_b128 v68, v[32:35] offset:7168
	s_waitcnt lgkmcnt(0)
	s_barrier
	global_load_dwordx4 v[4:7], v69, s[20:21]
	global_load_dwordx4 v[8:11], v69, s[20:21] offset:1024
	global_load_dwordx4 v[12:15], v69, s[20:21] offset:2048
	global_load_dwordx4 v[16:19], v69, s[20:21] offset:3072
	global_load_dwordx4 v[20:23], v69, s[22:23]
	global_load_dwordx4 v[24:27], v69, s[22:23] offset:1024
	global_load_dwordx4 v[28:31], v69, s[22:23] offset:2048
	global_load_dwordx4 v[32:35], v69, s[22:23] offset:3072
	s_add_u32 s20, s20, 0x1000
	s_addc_u32 s21, s21, 0
	s_add_u32 s22, s22, 0x1000
	s_addc_u32 s23, s23, 0
	s_waitcnt vmcnt(15)
	ds_write_b128 v68, v[36:39] offset:16384
	s_waitcnt vmcnt(14)
	ds_write_b128 v68, v[40:43] offset:17408
	s_waitcnt vmcnt(13)
	ds_write_b128 v68, v[44:47] offset:18432
	s_waitcnt vmcnt(12)
	ds_write_b128 v68, v[48:51] offset:19456
	s_waitcnt vmcnt(11)
	ds_write_b128 v68, v[52:55] offset:20480
	s_waitcnt vmcnt(10)
	ds_write_b128 v68, v[56:59] offset:21504
	s_waitcnt vmcnt(9)
	ds_write_b128 v68, v[60:63] offset:22528
	s_waitcnt vmcnt(8)
	ds_write_b128 v68, v[64:67] offset:23552
	s_waitcnt lgkmcnt(0)
	s_barrier
	global_load_dwordx4 v[36:39], v69, s[20:21]
	global_load_dwordx4 v[40:43], v69, s[20:21] offset:1024
	global_load_dwordx4 v[44:47], v69, s[20:21] offset:2048
	global_load_dwordx4 v[48:51], v69, s[20:21] offset:3072
	global_load_dwordx4 v[52:55], v69, s[22:23]
	global_load_dwordx4 v[56:59], v69, s[22:23] offset:1024
	global_load_dwordx4 v[60:63], v69, s[22:23] offset:2048
	global_load_dwordx4 v[64:67], v69, s[22:23] offset:3072
	s_add_u32 s20, s20, 0x1000
	s_addc_u32 s21, s21, 0
	s_add_u32 s22, s22, 0x1000
	s_addc_u32 s23, s23, 0
	s_waitcnt vmcnt(15)
	ds_write_b128 v68, v[4:7]
	s_waitcnt vmcnt(14)
	ds_write_b128 v68, v[8:11] offset:1024
	s_waitcnt vmcnt(13)
	ds_write_b128 v68, v[12:15] offset:2048
	s_waitcnt vmcnt(12)
	ds_write_b128 v68, v[16:19] offset:3072
	s_waitcnt vmcnt(11)
	ds_write_b128 v68, v[20:23] offset:4096
	s_waitcnt vmcnt(10)
	ds_write_b128 v68, v[24:27] offset:5120
	s_waitcnt vmcnt(9)
	ds_write_b128 v68, v[28:31] offset:6144
	s_waitcnt vmcnt(8)
	ds_write_b128 v68, v[32:35] offset:7168
	s_waitcnt lgkmcnt(0)
	s_barrier
	global_load_dwordx4 v[4:7], v69, s[20:21]
	global_load_dwordx4 v[8:11], v69, s[20:21] offset:1024
	global_load_dwordx4 v[12:15], v69, s[20:21] offset:2048
	global_load_dwordx4 v[16:19], v69, s[20:21] offset:3072
	global_load_dwordx4 v[20:23], v69, s[22:23]
	global_load_dwordx4 v[24:27], v69, s[22:23] offset:1024
	global_load_dwordx4 v[28:31], v69, s[22:23] offset:2048
	global_load_dwordx4 v[32:35], v69, s[22:23] offset:3072
	s_add_u32 s20, s20, 0x1000
	s_addc_u32 s21, s21, 0
	s_add_u32 s22, s22, 0x1000
	s_addc_u32 s23, s23, 0
	s_waitcnt vmcnt(15)
	ds_write_b128 v68, v[36:39] offset:16384
	s_waitcnt vmcnt(14)
	ds_write_b128 v68, v[40:43] offset:17408
	s_waitcnt vmcnt(13)
	ds_write_b128 v68, v[44:47] offset:18432
	s_waitcnt vmcnt(12)
	ds_write_b128 v68, v[48:51] offset:19456
	s_waitcnt vmcnt(11)
	ds_write_b128 v68, v[52:55] offset:20480
	s_waitcnt vmcnt(10)
	ds_write_b128 v68, v[56:59] offset:21504
	s_waitcnt vmcnt(9)
	ds_write_b128 v68, v[60:63] offset:22528
	s_waitcnt vmcnt(8)
	ds_write_b128 v68, v[64:67] offset:23552
	s_waitcnt lgkmcnt(0)
	s_barrier
	global_load_dwordx4 v[36:39], v69, s[20:21]
	global_load_dwordx4 v[40:43], v69, s[20:21] offset:1024
	global_load_dwordx4 v[44:47], v69, s[20:21] offset:2048
	global_load_dwordx4 v[48:51], v69, s[20:21] offset:3072
	global_load_dwordx4 v[52:55], v69, s[22:23]
	global_load_dwordx4 v[56:59], v69, s[22:23] offset:1024
	global_load_dwordx4 v[60:63], v69, s[22:23] offset:2048
	global_load_dwordx4 v[64:67], v69, s[22:23] offset:3072
	s_add_u32 s20, s20, 0x1000
	s_addc_u32 s21, s21, 0
	s_add_u32 s22, s22, 0x1000
	s_addc_u32 s23, s23, 0
	s_waitcnt vmcnt(15)
	ds_write_b128 v68, v[4:7]
	s_waitcnt vmcnt(14)
	ds_write_b128 v68, v[8:11] offset:1024
	s_waitcnt vmcnt(13)
	ds_write_b128 v68, v[12:15] offset:2048
	s_waitcnt vmcnt(12)
	ds_write_b128 v68, v[16:19] offset:3072
	s_waitcnt vmcnt(11)
	ds_write_b128 v68, v[20:23] offset:4096
	s_waitcnt vmcnt(10)
	ds_write_b128 v68, v[24:27] offset:5120
	s_waitcnt vmcnt(9)
	ds_write_b128 v68, v[28:31] offset:6144
	s_waitcnt vmcnt(8)
	ds_write_b128 v68, v[32:35] offset:7168
	s_waitcnt lgkmcnt(0)
	s_barrier
	global_load_dwordx4 v[4:7], v2, s[24:25] offset:-4096
	global_load_dwordx4 v[8:11], v2, s[24:25] offset:-2048
	global_load_dwordx4 v[12:15], v2, s[24:25]
	global_load_dwordx4 v[16:19], v2, s[24:25] offset:2048
	s_add_u32 s24, s24, 0x2000
	s_addc_u32 s25, s25, 0
	global_load_dwordx4 v[20:23], v2, s[24:25] offset:-4096
	global_load_dwordx4 v[24:27], v2, s[24:25] offset:-2048
	global_load_dwordx4 v[28:31], v2, s[24:25]
	global_load_dwordx4 v[32:35], v2, s[24:25] offset:2048
	s_waitcnt vmcnt(15)
	ds_write_b128 v68, v[36:39] offset:16384
	s_waitcnt vmcnt(14)
	ds_write_b128 v68, v[40:43] offset:17408
	s_waitcnt vmcnt(13)
	ds_write_b128 v68, v[44:47] offset:18432
	s_waitcnt vmcnt(12)
	ds_write_b128 v68, v[48:51] offset:19456
	s_waitcnt vmcnt(11)
	ds_write_b128 v68, v[52:55] offset:20480
	s_waitcnt vmcnt(10)
	ds_write_b128 v68, v[56:59] offset:21504
	s_waitcnt vmcnt(9)
	ds_write_b128 v68, v[60:63] offset:22528
	s_waitcnt vmcnt(8)
	ds_write_b128 v68, v[64:67] offset:23552
	s_waitcnt lgkmcnt(0)
	s_barrier
	s_waitcnt vmcnt(7)
	ds_write_b128 v2, v[4:7] offset:29696
	s_waitcnt vmcnt(6)
	ds_write_b128 v2, v[8:11] offset:31744
	s_waitcnt vmcnt(5)
	ds_write_b128 v2, v[12:15] offset:33792
	s_waitcnt vmcnt(4)
	ds_write_b128 v2, v[16:19] offset:35840
	s_waitcnt vmcnt(3)
	ds_write_b128 v2, v[20:23] offset:37888
	s_waitcnt vmcnt(2)
	ds_write_b128 v2, v[24:27] offset:39936
	s_waitcnt vmcnt(1)
	ds_write_b128 v2, v[28:31] offset:41984
	s_waitcnt vmcnt(0)
	ds_write_b128 v2, v[32:35] offset:44032
	s_waitcnt lgkmcnt(0)
	s_barrier
	s_endpgm
	s_nop 0
	s_nop 0
	s_nop 0
	s_nop 0
	s_nop 0
	s_endpgm
